# GLA pass 2: second gate-tile wait no longer waits for the O-tile store ack (vmcnt 1 -> 2)
# baseline (speedup 1.0000x reference)
; #define GAS __attribute__((address_space(1)))
; #define LAS __attribute__((address_space(3)))
; __device__ __forceinline__ f32x4 bf4lo(const v4u& w) { return (f32x4){bflo(w.x), bfhi(w.x), bflo(w.y), bfhi(w.y)}; }
; template <bool NEEDQ>
; __device__ __forceinline__ void write_stage(LAS unsigned char* lds, const Stage& st, int tid) {
;     ...
;     for (int i = 0; i < 4; ++i) { const int id = tid + 512 * i, row = id >> 5, cc = id & 31;
;         if (NEEDQ) *(LAS v4u*)(lds + OFF_Q + row * QS + cc * 16) = st.q[i]; *(LAS v4u*)(lds + OFF_K + row * KS + ((cc * 16) ^ (((row >> 3) & 1) << 7))) = st.k[i]; }
; #pragma unroll
;     for (int i = 0; i < 2; ++i) { const int id = tid + 512 * i, row = id >> 4, cc = id & 15; *(LAS v4u*)(lds + OFF_V + row * VS + ((cc * 16) ^ (((row >> 3) & 1) << 7))) = st.v[i]; }
;     if (tid < 256) *(LAS float*)(lds + OFF_G + 4 * tid) = expf(st.g);
; template <int PASS> ...
;     ...
;             for (int i = 0; i < 2; ++i) { const int id = tid + 512 * i, row = id >> 4, cc = id & 15;
;                 const v4u ov = *(const LAS v4u*)(lds + OFF_O + row * OS + cc * 16);
;                 const f32x4 a = bf4lo(ov), b = bf4hi(ov), ga = bf4lo(gpre[i]), gb = bf4hi(gpre[i]);
;                 float ss = (a.x * a.x + a.y * a.y) + (a.z * a.z + a.w * a.w) + (b.x * b.x + b.y * b.y) + (b.z * b.z + b.w * b.w);
;                 ss += __shfl_xor(ss, 1); ss += __shfl_xor(ss, 2); ss += __shfl_xor(ss, 4); ss += __shfl_xor(ss, 8);
;                 if (cc == 0) SS[(size_t)(tok0 + row) * 16 + h * 4 + s] = ss;
;                 const f32x4 ya = a * ga * hw0, yb = b * gb * hw1;
;                 v4u o; o.x = cvtpk(ya.x, ya.y); o.y = cvtpk(ya.z, ya.w); o.z = cvtpk(yb.x, yb.y); o.w = cvtpk(yb.z, yb.w);
;                 *(GAS v4u*)((GAS char*)OG + (size_t)tok0 * VD * 2 + i * 32 * VD * 2 + voff) = o; }
;         }
;         if (c + 1 < CPP) {
;             if (PASS == 1) {
;                 if ((c & 1) == 0) { write_stage<NQ>(lds, st0, tid); if (c + 3 < CPP) issue_loads<NQ>(st0, QP, KP, VB, BC, tok0 + 3 * CHK, h, s, tid, qkoff, voff); }
;                 else { write_stage<NQ>(lds, st1, tid); if (c + 3 < CPP) issue_loads<NQ>(st1, QP, KP, VB, BC, tok0 + 3 * CHK, h, s, tid, qkoff, voff); }
;             } else { write_stage<NQ>(lds, st0, tid); if (c + 2 < CPP) issue_loads<NQ>(st0, QP, KP, VB, BC, tok0 + 2 * CHK, h, s, tid, qkoff, voff); }
;             GLA_BAR();
.LBB0_428:
	s_or_b64 exec, exec, s[64:65]
	s_waitcnt vmcnt(2)
	v_lshlrev_b32_e32 v214, 16, v126
	v_and_b32_e32 v215, 0xffff0000, v126
	v_lshlrev_b32_e32 v126, 16, v127
	v_and_b32_e32 v127, 0xffff0000, v127
	v_lshlrev_b32_e32 v216, 16, v128
	v_and_b32_e32 v217, 0xffff0000, v128
	v_lshlrev_b32_e32 v128, 16, v129
	v_and_b32_e32 v129, 0xffff0000, v129
	v_pk_mul_f32 v[126:127], v[126:127], v[210:211]
	v_pk_mul_f32 v[212:213], v[214:215], v[212:213]
	v_pk_mul_f32 v[112:113], v[112:113], v[126:127]
	v_pk_mul_f32 v[126:127], v[216:217], v[148:149]
	v_pk_mul_f32 v[128:129], v[128:129], v[146:147]
	v_pk_mul_f32 v[110:111], v[110:111], v[212:213]
	v_pk_mul_f32 v[128:129], v[108:109], v[128:129]
	v_pk_mul_f32 v[108:109], v[106:107], v[126:127]
	v_cvt_pk_bf16_f32 v106, v110, v111
	v_cvt_pk_bf16_f32 v107, v112, v113
	v_cvt_pk_bf16_f32 v108, v108, v109
	v_cvt_pk_bf16_f32 v109, v128, v129
	s_cmpk_eq_i32 s50, 0x3c0
	global_store_dwordx4 v[208:209], v[106:109], off
	s_cbranch_scc1 .LBB0_423
	ds_write_b128 v235, v[42:45]
	ds_write_b128 v236, v[46:49] offset:33792
	ds_write_b128 v237, v[50:53]
	ds_write_b128 v238, v[58:61] offset:33792
	ds_write_b128 v235, v[62:65] offset:16896
	ds_write_b128 v236, v[66:69] offset:51200
	ds_write_b128 v239, v[74:77]
	ds_write_b128 v240, v[78:81] offset:33792
	ds_write_b128 v241, v[82:85]
	ds_write_b128 v242, v[86:89]
	s_and_saveexec_b64 s[64:65], s[6:7]
	s_cbranch_execz .LBB0_431
	v_mul_f32_e32 v106, 0x3fb8aa3b, v247
	v_rndne_f32_e32 v107, v106
	v_sub_f32_e32 v108, v106, v107
	v_fma_f32 v106, v247, s85, -v106
	v_fmac_f32_e32 v106, 0x32a5705f, v247
	v_add_f32_e32 v106, v108, v106
	v_cvt_i32_f32_e32 v107, v107
	v_exp_f32_e32 v106, v106
	v_cmp_ngt_f32_e32 vcc, s86, v247
	v_ldexp_f32 v106, v106, v107
	s_nop 0
	v_cndmask_b32_e32 v106, 0, v106, vcc
	v_cmp_nlt_f32_e32 vcc, s87, v247
	s_nop 1
	v_cndmask_b32_e32 v106, v243, v106, vcc
	ds_write_b32 v245, v106
